# removed s_nop 0 between DSA top-k count compare/add-carry pairs
# baseline (speedup 1.0000x reference)
.LBB0_838:
	v_add_u32_e32 v12, 1, v9
	v_cmp_gt_u32_e32 vcc, v10, v9
	s_nop 1
	v_cndmask_b32_e32 v10, v12, v10, vcc
	v_add_u32_e32 v12, -1, v11
	v_cmp_lt_u32_e32 vcc, v10, v11
	s_nop 1
	v_cndmask_b32_e32 v11, v12, v10, vcc
	v_mov_b32_e32 v10, v3
	v_cmp_ge_u32 vcc, v37, v11
	v_addc_co_u32 v10, vcc, 0, v10, vcc
	v_cmp_ge_u32 vcc, v36, v11
	v_addc_co_u32 v10, vcc, 0, v10, vcc
	v_cmp_ge_u32 vcc, v29, v11
	v_addc_co_u32 v10, vcc, 0, v10, vcc
	v_cmp_ge_u32 vcc, v28, v11
	v_addc_co_u32 v10, vcc, 0, v10, vcc
	v_cmp_ge_u32 vcc, v21, v11
	v_addc_co_u32 v10, vcc, 0, v10, vcc
	v_cmp_ge_u32 vcc, v20, v11
	v_addc_co_u32 v10, vcc, 0, v10, vcc
	v_cmp_ge_u32 vcc, v15, v11
	v_addc_co_u32 v10, vcc, 0, v10, vcc
	v_cmp_ge_u32 vcc, v14, v11
	v_addc_co_u32 v10, vcc, 0, v10, vcc
	v_cmp_ge_u32 vcc, v247, v11
	v_addc_co_u32 v10, vcc, 0, v10, vcc
	v_cmp_ge_u32 vcc, v246, v11
	v_addc_co_u32 v10, vcc, 0, v10, vcc
	v_cmp_ge_u32 vcc, v210, v11
	v_addc_co_u32 v10, vcc, 0, v10, vcc
	v_cmp_ge_u32 vcc, v245, v11
	v_addc_co_u32 v10, vcc, 0, v10, vcc
	v_cmp_ge_u32 vcc, v239, v11
	v_addc_co_u32 v10, vcc, 0, v10, vcc
	v_cmp_ge_u32 vcc, v244, v11
	v_addc_co_u32 v10, vcc, 0, v10, vcc
	v_cmp_ge_u32 vcc, v237, v11
	v_addc_co_u32 v10, vcc, 0, v10, vcc
	v_cmp_ge_u32 vcc, v243, v11
	v_addc_co_u32 v10, vcc, 0, v10, vcc
	v_cmp_ge_u32 vcc, v235, v11
	v_addc_co_u32 v10, vcc, 0, v10, vcc
	v_cmp_ge_u32 vcc, v242, v11
	v_addc_co_u32 v10, vcc, 0, v10, vcc
	v_cmp_ge_u32 vcc, v212, v11
	v_addc_co_u32 v10, vcc, 0, v10, vcc
	v_cmp_ge_u32 vcc, v241, v11
	v_addc_co_u32 v10, vcc, 0, v10, vcc
	v_cmp_ge_u32 vcc, v209, v11
	v_addc_co_u32 v10, vcc, 0, v10, vcc
	v_cmp_ge_u32 vcc, v240, v11
	v_addc_co_u32 v10, vcc, 0, v10, vcc
	v_cmp_ge_u32 vcc, v207, v11
	v_addc_co_u32 v10, vcc, 0, v10, vcc
	v_cmp_ge_u32 vcc, v238, v11
	v_addc_co_u32 v10, vcc, 0, v10, vcc
	v_cmp_ge_u32 vcc, v205, v11
	v_addc_co_u32 v10, vcc, 0, v10, vcc
	v_cmp_ge_u32 vcc, v236, v11
	v_addc_co_u32 v10, vcc, 0, v10, vcc
	v_cmp_ge_u32 vcc, v203, v11
	v_addc_co_u32 v10, vcc, 0, v10, vcc
	v_cmp_ge_u32 vcc, v213, v11
	v_addc_co_u32 v10, vcc, 0, v10, vcc
	v_cmp_ge_u32 vcc, v201, v11
	v_addc_co_u32 v10, vcc, 0, v10, vcc
	v_cmp_ge_u32 vcc, v211, v11
	v_addc_co_u32 v10, vcc, 0, v10, vcc
	v_cmp_ge_u32 vcc, v199, v11
	v_addc_co_u32 v10, vcc, 0, v10, vcc
	v_cmp_ge_u32 vcc, v208, v11
	v_addc_co_u32 v10, vcc, 0, v10, vcc
	s_and_saveexec_b64 s[68:69], s[8:9]
	s_cbranch_execz .LBB0_852
	v_cmp_ge_u32 vcc, v197, v11
	v_addc_co_u32 v10, vcc, 0, v10, vcc
	v_cmp_ge_u32 vcc, v206, v11
	v_addc_co_u32 v10, vcc, 0, v10, vcc
	v_cmp_ge_u32 vcc, v195, v11
	v_addc_co_u32 v10, vcc, 0, v10, vcc
	v_cmp_ge_u32 vcc, v204, v11
	v_addc_co_u32 v10, vcc, 0, v10, vcc
	v_cmp_ge_u32 vcc, v193, v11
	v_addc_co_u32 v10, vcc, 0, v10, vcc
	v_cmp_ge_u32 vcc, v202, v11
	v_addc_co_u32 v10, vcc, 0, v10, vcc
	v_cmp_ge_u32 vcc, v191, v11
	v_addc_co_u32 v10, vcc, 0, v10, vcc
	v_cmp_ge_u32 vcc, v200, v11
	v_addc_co_u32 v10, vcc, 0, v10, vcc
	v_cmp_ge_u32 vcc, v189, v11
	v_addc_co_u32 v10, vcc, 0, v10, vcc
	v_cmp_ge_u32 vcc, v198, v11
	v_addc_co_u32 v10, vcc, 0, v10, vcc
	v_cmp_ge_u32 vcc, v187, v11
	v_addc_co_u32 v10, vcc, 0, v10, vcc
	v_cmp_ge_u32 vcc, v196, v11
	v_addc_co_u32 v10, vcc, 0, v10, vcc
	v_cmp_ge_u32 vcc, v185, v11
	v_addc_co_u32 v10, vcc, 0, v10, vcc
	v_cmp_ge_u32 vcc, v194, v11
	v_addc_co_u32 v10, vcc, 0, v10, vcc
	v_cmp_ge_u32 vcc, v183, v11
	v_addc_co_u32 v10, vcc, 0, v10, vcc
	v_cmp_ge_u32 vcc, v192, v11
	v_addc_co_u32 v10, vcc, 0, v10, vcc
	v_cmp_ge_u32 vcc, v181, v11
	v_addc_co_u32 v10, vcc, 0, v10, vcc
	v_cmp_ge_u32 vcc, v190, v11
	v_addc_co_u32 v10, vcc, 0, v10, vcc
	v_cmp_ge_u32 vcc, v179, v11
	v_addc_co_u32 v10, vcc, 0, v10, vcc
	v_cmp_ge_u32 vcc, v188, v11
	v_addc_co_u32 v10, vcc, 0, v10, vcc
	v_cmp_ge_u32 vcc, v177, v11
	v_addc_co_u32 v10, vcc, 0, v10, vcc
	v_cmp_ge_u32 vcc, v186, v11
	v_addc_co_u32 v10, vcc, 0, v10, vcc
	v_cmp_ge_u32 vcc, v175, v11
	v_addc_co_u32 v10, vcc, 0, v10, vcc
	v_cmp_ge_u32 vcc, v184, v11
	v_addc_co_u32 v10, vcc, 0, v10, vcc
	v_cmp_ge_u32 vcc, v173, v11
	v_addc_co_u32 v10, vcc, 0, v10, vcc
	v_cmp_ge_u32 vcc, v182, v11
	v_addc_co_u32 v10, vcc, 0, v10, vcc
	v_cmp_ge_u32 vcc, v171, v11
	v_addc_co_u32 v10, vcc, 0, v10, vcc
	v_cmp_ge_u32 vcc, v180, v11
	v_addc_co_u32 v10, vcc, 0, v10, vcc
	v_cmp_ge_u32 vcc, v169, v11
	v_addc_co_u32 v10, vcc, 0, v10, vcc
	v_cmp_ge_u32 vcc, v178, v11
	v_addc_co_u32 v10, vcc, 0, v10, vcc
	v_cmp_ge_u32 vcc, v167, v11
	v_addc_co_u32 v10, vcc, 0, v10, vcc
	v_cmp_ge_u32 vcc, v176, v11
	v_addc_co_u32 v10, vcc, 0, v10, vcc
	s_or_b64 exec, exec, s[68:69]
	s_and_saveexec_b64 s[68:69], s[10:11]
	s_cbranch_execnz .LBB0_853

.LBB0_841:
	v_cmp_ge_u32 vcc, v132, v11
	v_addc_co_u32 v10, vcc, 0, v10, vcc
	v_cmp_ge_u32 vcc, v141, v11
	v_addc_co_u32 v10, vcc, 0, v10, vcc
	v_cmp_ge_u32 vcc, v73, v11
	v_addc_co_u32 v10, vcc, 0, v10, vcc
	v_cmp_ge_u32 vcc, v139, v11
	v_addc_co_u32 v10, vcc, 0, v10, vcc
	v_cmp_ge_u32 vcc, v47, v11
	v_addc_co_u32 v10, vcc, 0, v10, vcc
	v_cmp_ge_u32 vcc, v137, v11
	v_addc_co_u32 v10, vcc, 0, v10, vcc
	v_cmp_ge_u32 vcc, v42, v11
	v_addc_co_u32 v10, vcc, 0, v10, vcc
	v_cmp_ge_u32 vcc, v135, v11
	v_addc_co_u32 v10, vcc, 0, v10, vcc
	v_cmp_ge_u32 vcc, v40, v11
	v_addc_co_u32 v10, vcc, 0, v10, vcc
	v_cmp_ge_u32 vcc, v133, v11
	v_addc_co_u32 v10, vcc, 0, v10, vcc
	v_cmp_ge_u32 vcc, v38, v11
	v_addc_co_u32 v10, vcc, 0, v10, vcc
	v_cmp_ge_u32 vcc, v75, v11
	v_addc_co_u32 v10, vcc, 0, v10, vcc
	v_cmp_ge_u32 vcc, v34, v11
	v_addc_co_u32 v10, vcc, 0, v10, vcc
	v_cmp_ge_u32 vcc, v67, v11
	v_addc_co_u32 v10, vcc, 0, v10, vcc
	v_cmp_ge_u32 vcc, v32, v11
	v_addc_co_u32 v10, vcc, 0, v10, vcc
	v_cmp_ge_u32 vcc, v43, v11
	v_addc_co_u32 v10, vcc, 0, v10, vcc
	v_cmp_ge_u32 vcc, v30, v11
	v_addc_co_u32 v10, vcc, 0, v10, vcc
	v_cmp_ge_u32 vcc, v41, v11
	v_addc_co_u32 v10, vcc, 0, v10, vcc
	v_cmp_ge_u32 vcc, v26, v11
	v_addc_co_u32 v10, vcc, 0, v10, vcc
	v_cmp_ge_u32 vcc, v39, v11
	v_addc_co_u32 v10, vcc, 0, v10, vcc
	v_cmp_ge_u32 vcc, v24, v11
	v_addc_co_u32 v10, vcc, 0, v10, vcc
	v_cmp_ge_u32 vcc, v35, v11
	v_addc_co_u32 v10, vcc, 0, v10, vcc
	v_cmp_ge_u32 vcc, v22, v11
	v_addc_co_u32 v10, vcc, 0, v10, vcc
	v_cmp_ge_u32 vcc, v33, v11
	v_addc_co_u32 v10, vcc, 0, v10, vcc
	v_cmp_ge_u32 vcc, v19, v11
	v_addc_co_u32 v10, vcc, 0, v10, vcc
	v_cmp_ge_u32 vcc, v31, v11
	v_addc_co_u32 v10, vcc, 0, v10, vcc
	v_cmp_ge_u32 vcc, v18, v11
	v_addc_co_u32 v10, vcc, 0, v10, vcc
	v_cmp_ge_u32 vcc, v27, v11
	v_addc_co_u32 v10, vcc, 0, v10, vcc
	v_cmp_ge_u32 vcc, v17, v11
	v_addc_co_u32 v10, vcc, 0, v10, vcc
	v_cmp_ge_u32 vcc, v25, v11
	v_addc_co_u32 v10, vcc, 0, v10, vcc
	v_cmp_ge_u32 vcc, v16, v11
	v_addc_co_u32 v10, vcc, 0, v10, vcc
	v_cmp_ge_u32 vcc, v23, v11
	v_addc_co_u32 v10, vcc, 0, v10, vcc

.LBB0_853:
	v_cmp_ge_u32 vcc, v164, v11
	v_addc_co_u32 v10, vcc, 0, v10, vcc
	v_cmp_ge_u32 vcc, v174, v11
	v_addc_co_u32 v10, vcc, 0, v10, vcc
	v_cmp_ge_u32 vcc, v162, v11
	v_addc_co_u32 v10, vcc, 0, v10, vcc
	v_cmp_ge_u32 vcc, v172, v11
	v_addc_co_u32 v10, vcc, 0, v10, vcc
	v_cmp_ge_u32 vcc, v159, v11
	v_addc_co_u32 v10, vcc, 0, v10, vcc
	v_cmp_ge_u32 vcc, v170, v11
	v_addc_co_u32 v10, vcc, 0, v10, vcc
	v_cmp_ge_u32 vcc, v157, v11
	v_addc_co_u32 v10, vcc, 0, v10, vcc
	v_cmp_ge_u32 vcc, v168, v11
	v_addc_co_u32 v10, vcc, 0, v10, vcc
	v_cmp_ge_u32 vcc, v155, v11
	v_addc_co_u32 v10, vcc, 0, v10, vcc
	v_cmp_ge_u32 vcc, v166, v11
	v_addc_co_u32 v10, vcc, 0, v10, vcc
	v_cmp_ge_u32 vcc, v153, v11
	v_addc_co_u32 v10, vcc, 0, v10, vcc
	v_cmp_ge_u32 vcc, v165, v11
	v_addc_co_u32 v10, vcc, 0, v10, vcc
	v_cmp_ge_u32 vcc, v151, v11
	v_addc_co_u32 v10, vcc, 0, v10, vcc
	v_cmp_ge_u32 vcc, v163, v11
	v_addc_co_u32 v10, vcc, 0, v10, vcc
	v_cmp_ge_u32 vcc, v149, v11
	v_addc_co_u32 v10, vcc, 0, v10, vcc
	v_cmp_ge_u32 vcc, v160, v11
	v_addc_co_u32 v10, vcc, 0, v10, vcc
	v_cmp_ge_u32 vcc, v147, v11
	v_addc_co_u32 v10, vcc, 0, v10, vcc
	v_cmp_ge_u32 vcc, v158, v11
	v_addc_co_u32 v10, vcc, 0, v10, vcc
	v_cmp_ge_u32 vcc, v145, v11
	v_addc_co_u32 v10, vcc, 0, v10, vcc
	v_cmp_ge_u32 vcc, v156, v11
	v_addc_co_u32 v10, vcc, 0, v10, vcc
	v_cmp_ge_u32 vcc, v144, v11
	v_addc_co_u32 v10, vcc, 0, v10, vcc
	v_cmp_ge_u32 vcc, v154, v11
	v_addc_co_u32 v10, vcc, 0, v10, vcc
	v_cmp_ge_u32 vcc, v142, v11
	v_addc_co_u32 v10, vcc, 0, v10, vcc
	v_cmp_ge_u32 vcc, v152, v11
	v_addc_co_u32 v10, vcc, 0, v10, vcc
	v_cmp_ge_u32 vcc, v140, v11
	v_addc_co_u32 v10, vcc, 0, v10, vcc
	v_cmp_ge_u32 vcc, v150, v11
	v_addc_co_u32 v10, vcc, 0, v10, vcc
	v_cmp_ge_u32 vcc, v138, v11
	v_addc_co_u32 v10, vcc, 0, v10, vcc
	v_cmp_ge_u32 vcc, v148, v11
	v_addc_co_u32 v10, vcc, 0, v10, vcc
	v_cmp_ge_u32 vcc, v136, v11
	v_addc_co_u32 v10, vcc, 0, v10, vcc
	v_cmp_ge_u32 vcc, v146, v11
	v_addc_co_u32 v10, vcc, 0, v10, vcc
	v_cmp_ge_u32 vcc, v134, v11
	v_addc_co_u32 v10, vcc, 0, v10, vcc
	v_cmp_ge_u32 vcc, v143, v11
	v_addc_co_u32 v10, vcc, 0, v10, vcc
	s_or_b64 exec, exec, s[68:69]
	s_and_saveexec_b64 s[68:69], s[12:13]
	s_cbranch_execnz .LBB0_841
	s_branch .LBB0_842

.LBB0_857:
	s_xor_b64 s[2:3], s[62:63], -1
	s_and_b64 s[2:3], s[0:1], s[2:3]
	v_cndmask_b32_e64 v8, 1, v9, s[0:1]
	v_cndmask_b32_e64 v9, 0, 1, s[2:3]
	v_readlane_b32 s69, v253, 62
	v_cmp_ne_u32_e32 vcc, 0, v9
	s_cbranch_vccz .LBB0_871
	v_mov_b32_e32 v9, v3
	v_cmp_gt_u32 vcc, v37, v8
	v_addc_co_u32 v9, vcc, 0, v9, vcc
	v_cmp_gt_u32 vcc, v36, v8
	v_addc_co_u32 v9, vcc, 0, v9, vcc
	v_cmp_gt_u32 vcc, v29, v8
	v_addc_co_u32 v9, vcc, 0, v9, vcc
	v_cmp_gt_u32 vcc, v28, v8
	v_addc_co_u32 v9, vcc, 0, v9, vcc
	v_cmp_gt_u32 vcc, v21, v8
	v_addc_co_u32 v9, vcc, 0, v9, vcc
	v_cmp_gt_u32 vcc, v20, v8
	v_addc_co_u32 v9, vcc, 0, v9, vcc
	v_cmp_gt_u32 vcc, v15, v8
	v_addc_co_u32 v9, vcc, 0, v9, vcc
	v_cmp_gt_u32 vcc, v14, v8
	v_addc_co_u32 v9, vcc, 0, v9, vcc
	v_cmp_gt_u32 vcc, v247, v8
	v_addc_co_u32 v9, vcc, 0, v9, vcc
	v_cmp_gt_u32 vcc, v246, v8
	v_addc_co_u32 v9, vcc, 0, v9, vcc
	v_cmp_gt_u32 vcc, v210, v8
	v_addc_co_u32 v9, vcc, 0, v9, vcc
	v_cmp_gt_u32 vcc, v245, v8
	v_addc_co_u32 v9, vcc, 0, v9, vcc
	v_cmp_gt_u32 vcc, v239, v8
	v_addc_co_u32 v9, vcc, 0, v9, vcc
	v_cmp_gt_u32 vcc, v244, v8
	v_addc_co_u32 v9, vcc, 0, v9, vcc
	v_cmp_gt_u32 vcc, v237, v8
	v_addc_co_u32 v9, vcc, 0, v9, vcc
	v_cmp_gt_u32 vcc, v243, v8
	v_addc_co_u32 v9, vcc, 0, v9, vcc
	v_cmp_gt_u32 vcc, v235, v8
	v_addc_co_u32 v9, vcc, 0, v9, vcc
	v_cmp_gt_u32 vcc, v242, v8
	v_addc_co_u32 v9, vcc, 0, v9, vcc
	v_cmp_gt_u32 vcc, v212, v8
	v_addc_co_u32 v9, vcc, 0, v9, vcc
	v_cmp_gt_u32 vcc, v241, v8
	v_addc_co_u32 v9, vcc, 0, v9, vcc
	v_cmp_gt_u32 vcc, v209, v8
	v_addc_co_u32 v9, vcc, 0, v9, vcc
	v_cmp_gt_u32 vcc, v240, v8
	v_addc_co_u32 v9, vcc, 0, v9, vcc
	v_cmp_gt_u32 vcc, v207, v8
	v_addc_co_u32 v9, vcc, 0, v9, vcc
	v_cmp_gt_u32 vcc, v238, v8
	v_addc_co_u32 v9, vcc, 0, v9, vcc
	v_cmp_gt_u32 vcc, v205, v8
	v_addc_co_u32 v9, vcc, 0, v9, vcc
	v_cmp_gt_u32 vcc, v236, v8
	v_addc_co_u32 v9, vcc, 0, v9, vcc
	v_cmp_gt_u32 vcc, v203, v8
	v_addc_co_u32 v9, vcc, 0, v9, vcc
	v_cmp_gt_u32 vcc, v213, v8
	v_addc_co_u32 v9, vcc, 0, v9, vcc
	v_cmp_gt_u32 vcc, v201, v8
	v_addc_co_u32 v9, vcc, 0, v9, vcc
	v_cmp_gt_u32 vcc, v211, v8
	v_addc_co_u32 v9, vcc, 0, v9, vcc
	v_cmp_gt_u32 vcc, v199, v8
	v_addc_co_u32 v9, vcc, 0, v9, vcc
	v_cmp_gt_u32 vcc, v208, v8
	v_addc_co_u32 v9, vcc, 0, v9, vcc
	s_and_saveexec_b64 s[2:3], s[8:9]
	s_cbranch_execz .LBB0_867
	v_cmp_gt_u32 vcc, v197, v8
	v_addc_co_u32 v9, vcc, 0, v9, vcc
	v_cmp_gt_u32 vcc, v206, v8
	v_addc_co_u32 v9, vcc, 0, v9, vcc
	v_cmp_gt_u32 vcc, v195, v8
	v_addc_co_u32 v9, vcc, 0, v9, vcc
	v_cmp_gt_u32 vcc, v204, v8
	v_addc_co_u32 v9, vcc, 0, v9, vcc
	v_cmp_gt_u32 vcc, v193, v8
	v_addc_co_u32 v9, vcc, 0, v9, vcc
	v_cmp_gt_u32 vcc, v202, v8
	v_addc_co_u32 v9, vcc, 0, v9, vcc
	v_cmp_gt_u32 vcc, v191, v8
	v_addc_co_u32 v9, vcc, 0, v9, vcc
	v_cmp_gt_u32 vcc, v200, v8
	v_addc_co_u32 v9, vcc, 0, v9, vcc
	v_cmp_gt_u32 vcc, v189, v8
	v_addc_co_u32 v9, vcc, 0, v9, vcc
	v_cmp_gt_u32 vcc, v198, v8
	v_addc_co_u32 v9, vcc, 0, v9, vcc
	v_cmp_gt_u32 vcc, v187, v8
	v_addc_co_u32 v9, vcc, 0, v9, vcc
	v_cmp_gt_u32 vcc, v196, v8
	v_addc_co_u32 v9, vcc, 0, v9, vcc
	v_cmp_gt_u32 vcc, v185, v8
	v_addc_co_u32 v9, vcc, 0, v9, vcc
	v_cmp_gt_u32 vcc, v194, v8
	v_addc_co_u32 v9, vcc, 0, v9, vcc
	v_cmp_gt_u32 vcc, v183, v8
	v_addc_co_u32 v9, vcc, 0, v9, vcc
	v_cmp_gt_u32 vcc, v192, v8
	v_addc_co_u32 v9, vcc, 0, v9, vcc
	v_cmp_gt_u32 vcc, v181, v8
	v_addc_co_u32 v9, vcc, 0, v9, vcc
	v_cmp_gt_u32 vcc, v190, v8
	v_addc_co_u32 v9, vcc, 0, v9, vcc
	v_cmp_gt_u32 vcc, v179, v8
	v_addc_co_u32 v9, vcc, 0, v9, vcc
	v_cmp_gt_u32 vcc, v188, v8
	v_addc_co_u32 v9, vcc, 0, v9, vcc
	v_cmp_gt_u32 vcc, v177, v8
	v_addc_co_u32 v9, vcc, 0, v9, vcc
	v_cmp_gt_u32 vcc, v186, v8
	v_addc_co_u32 v9, vcc, 0, v9, vcc
	v_cmp_gt_u32 vcc, v175, v8
	v_addc_co_u32 v9, vcc, 0, v9, vcc
	v_cmp_gt_u32 vcc, v184, v8
	v_addc_co_u32 v9, vcc, 0, v9, vcc
	v_cmp_gt_u32 vcc, v173, v8
	v_addc_co_u32 v9, vcc, 0, v9, vcc
	v_cmp_gt_u32 vcc, v182, v8
	v_addc_co_u32 v9, vcc, 0, v9, vcc
	v_cmp_gt_u32 vcc, v171, v8
	v_addc_co_u32 v9, vcc, 0, v9, vcc
	v_cmp_gt_u32 vcc, v180, v8
	v_addc_co_u32 v9, vcc, 0, v9, vcc
	v_cmp_gt_u32 vcc, v169, v8
	v_addc_co_u32 v9, vcc, 0, v9, vcc
	v_cmp_gt_u32 vcc, v178, v8
	v_addc_co_u32 v9, vcc, 0, v9, vcc
	v_cmp_gt_u32 vcc, v167, v8
	v_addc_co_u32 v9, vcc, 0, v9, vcc
	v_cmp_gt_u32 vcc, v176, v8
	v_addc_co_u32 v9, vcc, 0, v9, vcc
	s_or_b64 exec, exec, s[2:3]
	s_and_saveexec_b64 s[2:3], s[10:11]
	s_cbranch_execnz .LBB0_868

.LBB0_861:
	v_cmp_gt_u32 vcc, v132, v8
	v_addc_co_u32 v9, vcc, 0, v9, vcc
	v_cmp_gt_u32 vcc, v141, v8
	v_addc_co_u32 v9, vcc, 0, v9, vcc
	v_cmp_gt_u32 vcc, v73, v8
	v_addc_co_u32 v9, vcc, 0, v9, vcc
	v_cmp_gt_u32 vcc, v139, v8
	v_addc_co_u32 v9, vcc, 0, v9, vcc
	v_cmp_gt_u32 vcc, v47, v8
	v_addc_co_u32 v9, vcc, 0, v9, vcc
	v_cmp_gt_u32 vcc, v137, v8
	v_addc_co_u32 v9, vcc, 0, v9, vcc
	v_cmp_gt_u32 vcc, v42, v8
	v_addc_co_u32 v9, vcc, 0, v9, vcc
	v_cmp_gt_u32 vcc, v135, v8
	v_addc_co_u32 v9, vcc, 0, v9, vcc
	v_cmp_gt_u32 vcc, v40, v8
	v_addc_co_u32 v9, vcc, 0, v9, vcc
	v_cmp_gt_u32 vcc, v133, v8
	v_addc_co_u32 v9, vcc, 0, v9, vcc
	v_cmp_gt_u32 vcc, v38, v8
	v_addc_co_u32 v9, vcc, 0, v9, vcc
	v_cmp_gt_u32 vcc, v75, v8
	v_addc_co_u32 v9, vcc, 0, v9, vcc
	v_cmp_gt_u32 vcc, v34, v8
	v_addc_co_u32 v9, vcc, 0, v9, vcc
	v_cmp_gt_u32 vcc, v67, v8
	v_addc_co_u32 v9, vcc, 0, v9, vcc
	v_cmp_gt_u32 vcc, v32, v8
	v_addc_co_u32 v9, vcc, 0, v9, vcc
	v_cmp_gt_u32 vcc, v43, v8
	v_addc_co_u32 v9, vcc, 0, v9, vcc
	v_cmp_gt_u32 vcc, v30, v8
	v_addc_co_u32 v9, vcc, 0, v9, vcc
	v_cmp_gt_u32 vcc, v41, v8
	v_addc_co_u32 v9, vcc, 0, v9, vcc
	v_cmp_gt_u32 vcc, v26, v8
	v_addc_co_u32 v9, vcc, 0, v9, vcc
	v_cmp_gt_u32 vcc, v39, v8
	v_addc_co_u32 v9, vcc, 0, v9, vcc
	v_cmp_gt_u32 vcc, v24, v8
	v_addc_co_u32 v9, vcc, 0, v9, vcc
	v_cmp_gt_u32 vcc, v35, v8
	v_addc_co_u32 v9, vcc, 0, v9, vcc
	v_cmp_gt_u32 vcc, v22, v8
	v_addc_co_u32 v9, vcc, 0, v9, vcc
	v_cmp_gt_u32 vcc, v33, v8
	v_addc_co_u32 v9, vcc, 0, v9, vcc
	v_cmp_gt_u32 vcc, v19, v8
	v_addc_co_u32 v9, vcc, 0, v9, vcc
	v_cmp_gt_u32 vcc, v31, v8
	v_addc_co_u32 v9, vcc, 0, v9, vcc
	v_cmp_gt_u32 vcc, v18, v8
	v_addc_co_u32 v9, vcc, 0, v9, vcc
	v_cmp_gt_u32 vcc, v27, v8
	v_addc_co_u32 v9, vcc, 0, v9, vcc
	v_cmp_gt_u32 vcc, v17, v8
	v_addc_co_u32 v9, vcc, 0, v9, vcc
	v_cmp_gt_u32 vcc, v25, v8
	v_addc_co_u32 v9, vcc, 0, v9, vcc
	v_cmp_gt_u32 vcc, v16, v8
	v_addc_co_u32 v9, vcc, 0, v9, vcc
	v_cmp_gt_u32 vcc, v23, v8
	v_addc_co_u32 v9, vcc, 0, v9, vcc
.LBB0_862:
	s_or_b64 exec, exec, s[2:3]
	v_mov_b32_e32 v11, v3
	v_cmp_eq_u32 vcc, v37, v8
	v_addc_co_u32 v11, vcc, 0, v11, vcc
	ds_bpermute_b32 v10, v74, v9
	v_cmp_eq_u32 vcc, v36, v8
	v_addc_co_u32 v11, vcc, 0, v11, vcc
	s_waitcnt lgkmcnt(0)
	v_add_u32_e32 v9, v10, v9
	v_cmp_eq_u32 vcc, v29, v8
	v_addc_co_u32 v11, vcc, 0, v11, vcc
	ds_bpermute_b32 v10, v76, v9
	v_cmp_eq_u32 vcc, v28, v8
	v_addc_co_u32 v11, vcc, 0, v11, vcc
	s_waitcnt lgkmcnt(0)
	v_add_u32_e32 v9, v9, v10
	v_cmp_eq_u32 vcc, v21, v8
	v_addc_co_u32 v11, vcc, 0, v11, vcc
	ds_bpermute_b32 v10, v77, v9
	v_cmp_eq_u32 vcc, v20, v8
	v_addc_co_u32 v11, vcc, 0, v11, vcc
	s_waitcnt lgkmcnt(0)
	v_add_u32_e32 v9, v9, v10
	v_cmp_eq_u32 vcc, v15, v8
	v_addc_co_u32 v11, vcc, 0, v11, vcc
	ds_bpermute_b32 v10, v78, v9
	v_cmp_eq_u32 vcc, v14, v8
	v_addc_co_u32 v11, vcc, 0, v11, vcc
	v_cmp_eq_u32 vcc, v247, v8
	v_addc_co_u32 v11, vcc, 0, v11, vcc
	v_cmp_eq_u32 vcc, v246, v8
	v_addc_co_u32 v11, vcc, 0, v11, vcc
	v_cmp_eq_u32 vcc, v210, v8
	v_addc_co_u32 v11, vcc, 0, v11, vcc
	v_cmp_eq_u32 vcc, v245, v8
	v_addc_co_u32 v11, vcc, 0, v11, vcc
	v_cmp_eq_u32 vcc, v239, v8
	v_addc_co_u32 v11, vcc, 0, v11, vcc
	v_cmp_eq_u32 vcc, v244, v8
	v_addc_co_u32 v11, vcc, 0, v11, vcc
	v_cmp_eq_u32 vcc, v237, v8
	v_addc_co_u32 v11, vcc, 0, v11, vcc
	v_cmp_eq_u32 vcc, v243, v8
	v_addc_co_u32 v11, vcc, 0, v11, vcc
	v_cmp_eq_u32 vcc, v235, v8
	v_addc_co_u32 v11, vcc, 0, v11, vcc
	v_cmp_eq_u32 vcc, v242, v8
	v_addc_co_u32 v11, vcc, 0, v11, vcc
	v_cmp_eq_u32 vcc, v212, v8
	v_addc_co_u32 v11, vcc, 0, v11, vcc
	v_cmp_eq_u32 vcc, v241, v8
	v_addc_co_u32 v11, vcc, 0, v11, vcc
	v_cmp_eq_u32 vcc, v209, v8
	v_addc_co_u32 v11, vcc, 0, v11, vcc
	v_cmp_eq_u32 vcc, v240, v8
	v_addc_co_u32 v11, vcc, 0, v11, vcc
	v_cmp_eq_u32 vcc, v207, v8
	v_addc_co_u32 v11, vcc, 0, v11, vcc
	v_cmp_eq_u32 vcc, v238, v8
	v_addc_co_u32 v11, vcc, 0, v11, vcc
	v_cmp_eq_u32 vcc, v205, v8
	v_addc_co_u32 v11, vcc, 0, v11, vcc
	v_cmp_eq_u32 vcc, v236, v8
	v_addc_co_u32 v11, vcc, 0, v11, vcc
	v_cmp_eq_u32 vcc, v203, v8
	v_addc_co_u32 v11, vcc, 0, v11, vcc
	v_cmp_eq_u32 vcc, v213, v8
	v_addc_co_u32 v11, vcc, 0, v11, vcc
	v_cmp_eq_u32 vcc, v201, v8
	v_addc_co_u32 v11, vcc, 0, v11, vcc
	v_cmp_eq_u32 vcc, v211, v8
	v_addc_co_u32 v11, vcc, 0, v11, vcc
	v_cmp_eq_u32 vcc, v199, v8
	v_addc_co_u32 v11, vcc, 0, v11, vcc
	v_cmp_eq_u32 vcc, v208, v8
	v_addc_co_u32 v11, vcc, 0, v11, vcc
	s_and_saveexec_b64 s[2:3], s[8:9]
	s_cbranch_execz .LBB0_869
	v_cmp_eq_u32 vcc, v197, v8
	v_addc_co_u32 v11, vcc, 0, v11, vcc
	v_cmp_eq_u32 vcc, v206, v8
	v_addc_co_u32 v11, vcc, 0, v11, vcc
	v_cmp_eq_u32 vcc, v195, v8
	v_addc_co_u32 v11, vcc, 0, v11, vcc
	v_cmp_eq_u32 vcc, v204, v8
	v_addc_co_u32 v11, vcc, 0, v11, vcc
	v_cmp_eq_u32 vcc, v193, v8
	v_addc_co_u32 v11, vcc, 0, v11, vcc
	v_cmp_eq_u32 vcc, v202, v8
	v_addc_co_u32 v11, vcc, 0, v11, vcc
	v_cmp_eq_u32 vcc, v191, v8
	v_addc_co_u32 v11, vcc, 0, v11, vcc
	v_cmp_eq_u32 vcc, v200, v8
	v_addc_co_u32 v11, vcc, 0, v11, vcc
	v_cmp_eq_u32 vcc, v189, v8
	v_addc_co_u32 v11, vcc, 0, v11, vcc
	v_cmp_eq_u32 vcc, v198, v8
	v_addc_co_u32 v11, vcc, 0, v11, vcc
	v_cmp_eq_u32 vcc, v187, v8
	v_addc_co_u32 v11, vcc, 0, v11, vcc
	v_cmp_eq_u32 vcc, v196, v8
	v_addc_co_u32 v11, vcc, 0, v11, vcc
	v_cmp_eq_u32 vcc, v185, v8
	v_addc_co_u32 v11, vcc, 0, v11, vcc
	v_cmp_eq_u32 vcc, v194, v8
	v_addc_co_u32 v11, vcc, 0, v11, vcc
	v_cmp_eq_u32 vcc, v183, v8
	v_addc_co_u32 v11, vcc, 0, v11, vcc
	v_cmp_eq_u32 vcc, v192, v8
	v_addc_co_u32 v11, vcc, 0, v11, vcc
	v_cmp_eq_u32 vcc, v181, v8
	v_addc_co_u32 v11, vcc, 0, v11, vcc
	v_cmp_eq_u32 vcc, v190, v8
	v_addc_co_u32 v11, vcc, 0, v11, vcc
	v_cmp_eq_u32 vcc, v179, v8
	v_addc_co_u32 v11, vcc, 0, v11, vcc
	v_cmp_eq_u32 vcc, v188, v8
	v_addc_co_u32 v11, vcc, 0, v11, vcc
	v_cmp_eq_u32 vcc, v177, v8
	v_addc_co_u32 v11, vcc, 0, v11, vcc
	v_cmp_eq_u32 vcc, v186, v8
	v_addc_co_u32 v11, vcc, 0, v11, vcc
	v_cmp_eq_u32 vcc, v175, v8
	v_addc_co_u32 v11, vcc, 0, v11, vcc
	v_cmp_eq_u32 vcc, v184, v8
	v_addc_co_u32 v11, vcc, 0, v11, vcc
	v_cmp_eq_u32 vcc, v173, v8
	v_addc_co_u32 v11, vcc, 0, v11, vcc
	v_cmp_eq_u32 vcc, v182, v8
	v_addc_co_u32 v11, vcc, 0, v11, vcc
	v_cmp_eq_u32 vcc, v171, v8
	v_addc_co_u32 v11, vcc, 0, v11, vcc
	v_cmp_eq_u32 vcc, v180, v8
	v_addc_co_u32 v11, vcc, 0, v11, vcc
	v_cmp_eq_u32 vcc, v169, v8
	v_addc_co_u32 v11, vcc, 0, v11, vcc
	v_cmp_eq_u32 vcc, v178, v8
	v_addc_co_u32 v11, vcc, 0, v11, vcc
	v_cmp_eq_u32 vcc, v167, v8
	v_addc_co_u32 v11, vcc, 0, v11, vcc
	v_cmp_eq_u32 vcc, v176, v8
	v_addc_co_u32 v11, vcc, 0, v11, vcc
	s_or_b64 exec, exec, s[2:3]
	s_and_saveexec_b64 s[2:3], s[10:11]
	s_cbranch_execnz .LBB0_870

.LBB0_865:
	v_cmp_eq_u32 vcc, v132, v8
	v_addc_co_u32 v11, vcc, 0, v11, vcc
	v_cmp_eq_u32 vcc, v141, v8
	v_addc_co_u32 v11, vcc, 0, v11, vcc
	v_cmp_eq_u32 vcc, v73, v8
	v_addc_co_u32 v11, vcc, 0, v11, vcc
	v_cmp_eq_u32 vcc, v139, v8
	v_addc_co_u32 v11, vcc, 0, v11, vcc
	v_cmp_eq_u32 vcc, v47, v8
	v_addc_co_u32 v11, vcc, 0, v11, vcc
	v_cmp_eq_u32 vcc, v137, v8
	v_addc_co_u32 v11, vcc, 0, v11, vcc
	v_cmp_eq_u32 vcc, v42, v8
	v_addc_co_u32 v11, vcc, 0, v11, vcc
	v_cmp_eq_u32 vcc, v135, v8
	v_addc_co_u32 v11, vcc, 0, v11, vcc
	v_cmp_eq_u32 vcc, v40, v8
	v_addc_co_u32 v11, vcc, 0, v11, vcc
	v_cmp_eq_u32 vcc, v133, v8
	v_addc_co_u32 v11, vcc, 0, v11, vcc
	v_cmp_eq_u32 vcc, v38, v8
	v_addc_co_u32 v11, vcc, 0, v11, vcc
	v_cmp_eq_u32 vcc, v75, v8
	v_addc_co_u32 v11, vcc, 0, v11, vcc
	v_cmp_eq_u32 vcc, v34, v8
	v_addc_co_u32 v11, vcc, 0, v11, vcc
	v_cmp_eq_u32 vcc, v67, v8
	v_addc_co_u32 v11, vcc, 0, v11, vcc
	v_cmp_eq_u32 vcc, v32, v8
	v_addc_co_u32 v11, vcc, 0, v11, vcc
	v_cmp_eq_u32 vcc, v43, v8
	v_addc_co_u32 v11, vcc, 0, v11, vcc
	v_cmp_eq_u32 vcc, v30, v8
	v_addc_co_u32 v11, vcc, 0, v11, vcc
	v_cmp_eq_u32 vcc, v41, v8
	v_addc_co_u32 v11, vcc, 0, v11, vcc
	v_cmp_eq_u32 vcc, v26, v8
	v_addc_co_u32 v11, vcc, 0, v11, vcc
	v_cmp_eq_u32 vcc, v39, v8
	v_addc_co_u32 v11, vcc, 0, v11, vcc
	v_cmp_eq_u32 vcc, v24, v8
	v_addc_co_u32 v11, vcc, 0, v11, vcc
	v_cmp_eq_u32 vcc, v35, v8
	v_addc_co_u32 v11, vcc, 0, v11, vcc
	v_cmp_eq_u32 vcc, v22, v8
	v_addc_co_u32 v11, vcc, 0, v11, vcc
	v_cmp_eq_u32 vcc, v33, v8
	v_addc_co_u32 v11, vcc, 0, v11, vcc
	v_cmp_eq_u32 vcc, v19, v8
	v_addc_co_u32 v11, vcc, 0, v11, vcc
	v_cmp_eq_u32 vcc, v31, v8
	v_addc_co_u32 v11, vcc, 0, v11, vcc
	v_cmp_eq_u32 vcc, v18, v8
	v_addc_co_u32 v11, vcc, 0, v11, vcc
	v_cmp_eq_u32 vcc, v27, v8
	v_addc_co_u32 v11, vcc, 0, v11, vcc
	v_cmp_eq_u32 vcc, v17, v8
	v_addc_co_u32 v11, vcc, 0, v11, vcc
	v_cmp_eq_u32 vcc, v25, v8
	v_addc_co_u32 v11, vcc, 0, v11, vcc
	v_cmp_eq_u32 vcc, v16, v8
	v_addc_co_u32 v11, vcc, 0, v11, vcc
	v_cmp_eq_u32 vcc, v23, v8
	v_addc_co_u32 v11, vcc, 0, v11, vcc

.LBB0_868:
	v_cmp_gt_u32 vcc, v164, v8
	v_addc_co_u32 v9, vcc, 0, v9, vcc
	v_cmp_gt_u32 vcc, v174, v8
	v_addc_co_u32 v9, vcc, 0, v9, vcc
	v_cmp_gt_u32 vcc, v162, v8
	v_addc_co_u32 v9, vcc, 0, v9, vcc
	v_cmp_gt_u32 vcc, v172, v8
	v_addc_co_u32 v9, vcc, 0, v9, vcc
	v_cmp_gt_u32 vcc, v159, v8
	v_addc_co_u32 v9, vcc, 0, v9, vcc
	v_cmp_gt_u32 vcc, v170, v8
	v_addc_co_u32 v9, vcc, 0, v9, vcc
	v_cmp_gt_u32 vcc, v157, v8
	v_addc_co_u32 v9, vcc, 0, v9, vcc
	v_cmp_gt_u32 vcc, v168, v8
	v_addc_co_u32 v9, vcc, 0, v9, vcc
	v_cmp_gt_u32 vcc, v155, v8
	v_addc_co_u32 v9, vcc, 0, v9, vcc
	v_cmp_gt_u32 vcc, v166, v8
	v_addc_co_u32 v9, vcc, 0, v9, vcc
	v_cmp_gt_u32 vcc, v153, v8
	v_addc_co_u32 v9, vcc, 0, v9, vcc
	v_cmp_gt_u32 vcc, v165, v8
	v_addc_co_u32 v9, vcc, 0, v9, vcc
	v_cmp_gt_u32 vcc, v151, v8
	v_addc_co_u32 v9, vcc, 0, v9, vcc
	v_cmp_gt_u32 vcc, v163, v8
	v_addc_co_u32 v9, vcc, 0, v9, vcc
	v_cmp_gt_u32 vcc, v149, v8
	v_addc_co_u32 v9, vcc, 0, v9, vcc
	v_cmp_gt_u32 vcc, v160, v8
	v_addc_co_u32 v9, vcc, 0, v9, vcc
	v_cmp_gt_u32 vcc, v147, v8
	v_addc_co_u32 v9, vcc, 0, v9, vcc
	v_cmp_gt_u32 vcc, v158, v8
	v_addc_co_u32 v9, vcc, 0, v9, vcc
	v_cmp_gt_u32 vcc, v145, v8
	v_addc_co_u32 v9, vcc, 0, v9, vcc
	v_cmp_gt_u32 vcc, v156, v8
	v_addc_co_u32 v9, vcc, 0, v9, vcc
	v_cmp_gt_u32 vcc, v144, v8
	v_addc_co_u32 v9, vcc, 0, v9, vcc
	v_cmp_gt_u32 vcc, v154, v8
	v_addc_co_u32 v9, vcc, 0, v9, vcc
	v_cmp_gt_u32 vcc, v142, v8
	v_addc_co_u32 v9, vcc, 0, v9, vcc
	v_cmp_gt_u32 vcc, v152, v8
	v_addc_co_u32 v9, vcc, 0, v9, vcc
	v_cmp_gt_u32 vcc, v140, v8
	v_addc_co_u32 v9, vcc, 0, v9, vcc
	v_cmp_gt_u32 vcc, v150, v8
	v_addc_co_u32 v9, vcc, 0, v9, vcc
	v_cmp_gt_u32 vcc, v138, v8
	v_addc_co_u32 v9, vcc, 0, v9, vcc
	v_cmp_gt_u32 vcc, v148, v8
	v_addc_co_u32 v9, vcc, 0, v9, vcc
	v_cmp_gt_u32 vcc, v136, v8
	v_addc_co_u32 v9, vcc, 0, v9, vcc
	v_cmp_gt_u32 vcc, v146, v8
	v_addc_co_u32 v9, vcc, 0, v9, vcc
	v_cmp_gt_u32 vcc, v134, v8
	v_addc_co_u32 v9, vcc, 0, v9, vcc
	v_cmp_gt_u32 vcc, v143, v8
	v_addc_co_u32 v9, vcc, 0, v9, vcc
	s_or_b64 exec, exec, s[2:3]
	s_and_saveexec_b64 s[2:3], s[12:13]
	s_cbranch_execnz .LBB0_861
	s_branch .LBB0_862

.LBB0_870:
	v_cmp_eq_u32 vcc, v164, v8
	v_addc_co_u32 v11, vcc, 0, v11, vcc
	v_cmp_eq_u32 vcc, v174, v8
	v_addc_co_u32 v11, vcc, 0, v11, vcc
	v_cmp_eq_u32 vcc, v162, v8
	v_addc_co_u32 v11, vcc, 0, v11, vcc
	v_cmp_eq_u32 vcc, v172, v8
	v_addc_co_u32 v11, vcc, 0, v11, vcc
	v_cmp_eq_u32 vcc, v159, v8
	v_addc_co_u32 v11, vcc, 0, v11, vcc
	v_cmp_eq_u32 vcc, v170, v8
	v_addc_co_u32 v11, vcc, 0, v11, vcc
	v_cmp_eq_u32 vcc, v157, v8
	v_addc_co_u32 v11, vcc, 0, v11, vcc
	v_cmp_eq_u32 vcc, v168, v8
	v_addc_co_u32 v11, vcc, 0, v11, vcc
	v_cmp_eq_u32 vcc, v155, v8
	v_addc_co_u32 v11, vcc, 0, v11, vcc
	v_cmp_eq_u32 vcc, v166, v8
	v_addc_co_u32 v11, vcc, 0, v11, vcc
	v_cmp_eq_u32 vcc, v153, v8
	v_addc_co_u32 v11, vcc, 0, v11, vcc
	v_cmp_eq_u32 vcc, v165, v8
	v_addc_co_u32 v11, vcc, 0, v11, vcc
	v_cmp_eq_u32 vcc, v151, v8
	v_addc_co_u32 v11, vcc, 0, v11, vcc
	v_cmp_eq_u32 vcc, v163, v8
	v_addc_co_u32 v11, vcc, 0, v11, vcc
	v_cmp_eq_u32 vcc, v149, v8
	v_addc_co_u32 v11, vcc, 0, v11, vcc
	v_cmp_eq_u32 vcc, v160, v8
	v_addc_co_u32 v11, vcc, 0, v11, vcc
	v_cmp_eq_u32 vcc, v147, v8
	v_addc_co_u32 v11, vcc, 0, v11, vcc
	v_cmp_eq_u32 vcc, v158, v8
	v_addc_co_u32 v11, vcc, 0, v11, vcc
	v_cmp_eq_u32 vcc, v145, v8
	v_addc_co_u32 v11, vcc, 0, v11, vcc
	v_cmp_eq_u32 vcc, v156, v8
	v_addc_co_u32 v11, vcc, 0, v11, vcc
	v_cmp_eq_u32 vcc, v144, v8
	v_addc_co_u32 v11, vcc, 0, v11, vcc
	v_cmp_eq_u32 vcc, v154, v8
	v_addc_co_u32 v11, vcc, 0, v11, vcc
	v_cmp_eq_u32 vcc, v142, v8
	v_addc_co_u32 v11, vcc, 0, v11, vcc
	v_cmp_eq_u32 vcc, v152, v8
	v_addc_co_u32 v11, vcc, 0, v11, vcc
	v_cmp_eq_u32 vcc, v140, v8
	v_addc_co_u32 v11, vcc, 0, v11, vcc
	v_cmp_eq_u32 vcc, v150, v8
	v_addc_co_u32 v11, vcc, 0, v11, vcc
	v_cmp_eq_u32 vcc, v138, v8
	v_addc_co_u32 v11, vcc, 0, v11, vcc
	v_cmp_eq_u32 vcc, v148, v8
	v_addc_co_u32 v11, vcc, 0, v11, vcc
	v_cmp_eq_u32 vcc, v136, v8
	v_addc_co_u32 v11, vcc, 0, v11, vcc
	v_cmp_eq_u32 vcc, v146, v8
	v_addc_co_u32 v11, vcc, 0, v11, vcc
	v_cmp_eq_u32 vcc, v134, v8
	v_addc_co_u32 v11, vcc, 0, v11, vcc
	v_cmp_eq_u32 vcc, v143, v8
	v_addc_co_u32 v11, vcc, 0, v11, vcc
	s_or_b64 exec, exec, s[2:3]
	s_and_saveexec_b64 s[2:3], s[12:13]
	s_cbranch_execnz .LBB0_865
	s_branch .LBB0_866
